# mixer-A first head: later heads' 12 bias reads moved into the QK MFMA->VALU wait slot (first QK MFMAs issue ~24 slots earlier, s_nop 4/1 removed)
# baseline (speedup 1.0000x reference)
.LBB0_806:
	s_min_u32 s8, s7, 8
	s_add_i32 s8, s8, s6
	v_med3_i32 v5, s8, 0, v184
	v_lshl_or_b32 v2, v5, 11, v160
	v_lshl_add_u64 v[94:95], v[172:173], 0, v[2:3]
	v_lshlrev_b32_e32 v2, 12, v5
	v_lshl_add_u64 v[122:123], v[174:175], 0, v[2:3]
	global_load_dwordx4 v[90:93], v[94:95], off
	s_nop 0
	global_load_dwordx4 v[94:97], v[94:95], off offset:1024
	s_nop 0
	global_load_dwordx4 v[106:109], v[122:123], off
	global_load_dwordx4 v[110:113], v[122:123], off offset:1024
	global_load_dwordx4 v[118:121], v[122:123], off offset:2048
	s_nop 0
	global_load_dwordx4 v[122:125], v[122:123], off offset:3072
	s_add_i32 s8, s6, s7
	s_add_i32 s8, s8, -1
	s_cmpk_gt_u32 s8, 0xff
	s_cbranch_scc1 .LBB0_816
	ds_read2_b32 v[214:215], v190 offset1:1
	ds_read2_b32 v[216:217], v190 offset0:2 offset1:3
	ds_read2_b32 v[218:219], v190 offset0:16 offset1:17
	ds_read2_b32 v[220:221], v190 offset0:18 offset1:19
	s_waitcnt vmcnt(11) lgkmcnt(2)
	v_mfma_f32_16x16x32_fp8_fp8 v[134:137], v[130:131], v[70:71], v[214:217]
	v_mfma_f32_16x16x32_fp8_fp8 v[138:141], v[132:133], v[72:73], v[134:137]
	s_waitcnt vmcnt(10) lgkmcnt(0)
	v_mfma_f32_16x16x32_fp8_fp8 v[134:137], v[126:127], v[70:71], v[218:221]
	v_mfma_f32_16x16x32_fp8_fp8 v[134:137], v[128:129], v[72:73], v[134:137]
	v_add_u32_e32 v246, 0x504, v190
	v_add_u32_e32 v247, 0x50c, v190
	ds_read2_b32 v[222:223], v246 offset1:1
	ds_read2_b32 v[224:225], v247 offset1:1
	v_add_u32_e32 v246, 0x544, v190
	v_add_u32_e32 v247, 0x54c, v190
	ds_read2_b32 v[226:227], v246 offset1:1
	ds_read2_b32 v[228:229], v247 offset1:1
	v_add_u32_e32 v246, 0xa08, v190
	v_add_u32_e32 v247, 0xa10, v190
	ds_read2_b32 v[230:231], v246 offset1:1
	ds_read2_b32 v[232:233], v247 offset1:1
	v_add_u32_e32 v246, 0xa48, v190
	v_add_u32_e32 v247, 0xa50, v190
	ds_read2_b32 v[234:235], v246 offset1:1
	ds_read2_b32 v[236:237], v247 offset1:1
	v_add_u32_e32 v246, 0xf0c, v190
	v_add_u32_e32 v247, 0xf14, v190
	ds_read2_b32 v[238:239], v246 offset1:1
	ds_read2_b32 v[240:241], v247 offset1:1
	v_add_u32_e32 v246, 0xf4c, v190
	v_add_u32_e32 v247, 0xf54, v190
	ds_read2_b32 v[242:243], v246 offset1:1
	ds_read2_b32 v[244:245], v247 offset1:1
	v_max3_f32 v2, v138, v139, v140
	v_max3_f32 v191, v141, v134, v135
	v_max3_f32 v2, v2, v136, v137
	v_max_f32_e32 v2, v2, v191
	v_mov_b32_e32 v5, v2
	s_nop 1
	v_permlane16_swap_b32_e32 v2, v5
	v_max_f32_e32 v2, v2, v5
	v_mov_b32_e32 v5, v2
	s_nop 1
	v_permlane32_swap_b32_e32 v2, v5
	v_max_f32_e32 v2, v2, v5
	v_cmp_gt_f32_e32 vcc, v2, v176
	s_cbranch_vccz .LBB0_809
	v_max_f32_e32 v2, v2, v2
	v_max_f32_e32 v5, v176, v176
	v_max_f32_e32 v5, v5, v2
	v_sub_f32_e32 v2, v176, v5
	v_exp_f32_e32 v2, v2
	v_mov_b32_e32 v176, v5
	v_mul_f32_e32 v4, v4, v2
	v_pk_mul_f32 v[68:69], v[68:69], v[2:3] op_sel_hi:[1,0]
	v_pk_mul_f32 v[66:67], v[66:67], v[2:3] op_sel_hi:[1,0]
	v_pk_mul_f32 v[64:65], v[64:65], v[2:3] op_sel_hi:[1,0]
	v_pk_mul_f32 v[62:63], v[62:63], v[2:3] op_sel_hi:[1,0]
	v_pk_mul_f32 v[60:61], v[60:61], v[2:3] op_sel_hi:[1,0]
	v_pk_mul_f32 v[58:59], v[58:59], v[2:3] op_sel_hi:[1,0]
	v_pk_mul_f32 v[56:57], v[56:57], v[2:3] op_sel_hi:[1,0]
	v_pk_mul_f32 v[54:55], v[54:55], v[2:3] op_sel_hi:[1,0]
